# v33 + attention tile loop: scalar fma pairs and the two row-sum add chains packed (v_pk_fma_f32 / v_pk_add_f32)
# baseline (speedup 1.0000x reference)
.LBB0_1217:
	s_add_i32 s2, s77, -2
	v_lshl_add_u64 v[182:183], s[82:83], 0, v[180:181]
	v_add_co_u32_e32 v96, vcc, s94, v182
	v_lshl_add_u64 v[138:139], s[82:83], 0, v[128:129]
	s_nop 0
	v_addc_co_u32_e32 v97, vcc, 0, v183, vcc
	v_add_co_u32_e32 v98, vcc, s94, v138
	s_nop 1
	v_addc_co_u32_e32 v99, vcc, 0, v139, vcc
	global_load_dwordx4 v[130:133], v[96:97], off
	global_load_dwordx4 v[134:137], v[98:99], off
	v_add_co_u32_e32 v96, vcc, s95, v182
	s_nop 1
	v_addc_co_u32_e32 v97, vcc, 0, v183, vcc
	v_add_co_u32_e32 v98, vcc, s95, v138
	s_nop 1
	v_addc_co_u32_e32 v99, vcc, 0, v139, vcc
	global_load_dwordx4 v[168:171], v[96:97], off
	global_load_dwordx4 v[176:179], v[98:99], off
	ds_read_b128 v[96:99], v195 offset:49152
	ds_read_b128 v[100:103], v195 offset:57344
	ds_read_b128 v[204:207], v196 offset:49152
	ds_read_b128 v[214:217], v196 offset:57344
	v_exp_f32_e32 v218, v87
	v_exp_f32_e32 v219, v88
	s_waitcnt lgkmcnt(3)
	v_mfma_f32_32x32x16_bf16 v[112:127], v[96:99], v[140:143], 0
	v_exp_f32_e32 v220, v89
	v_exp_f32_e32 v221, v90
	v_exp_f32_e32 v222, v91
	v_exp_f32_e32 v223, v92
	v_exp_f32_e32 v224, v93
	v_exp_f32_e32 v225, v94
	v_exp_f32_e32 v95, v95
	s_waitcnt lgkmcnt(2)
	v_mfma_f32_32x32x16_bf16 v[96:111], v[100:103], v[140:143], 0
	s_waitcnt lgkmcnt(1)
	v_mfma_f32_32x32x16_bf16 v[112:127], v[204:207], v[144:147], v[112:127]
	s_waitcnt lgkmcnt(0)
	v_mfma_f32_32x32x16_bf16 v[96:111], v[214:217], v[144:147], v[96:111]
	ds_read_b128 v[204:207], v197 offset:49152
	ds_read_b128 v[214:217], v197 offset:57344
	s_waitcnt lgkmcnt(1)
	v_mfma_f32_32x32x16_bf16 v[112:127], v[204:207], v[148:151], v[112:127]
	s_waitcnt lgkmcnt(0)
	v_mfma_f32_32x32x16_bf16 v[96:111], v[214:217], v[148:151], v[96:111]
	ds_read_b128 v[204:207], v198 offset:49152
	ds_read_b128 v[214:217], v198 offset:57344
	s_waitcnt lgkmcnt(1)
	v_mfma_f32_32x32x16_bf16 v[112:127], v[204:207], v[152:155], v[112:127]
	s_waitcnt lgkmcnt(0)
	v_mfma_f32_32x32x16_bf16 v[96:111], v[214:217], v[152:155], v[96:111]
	ds_read_b128 v[204:207], v195 offset:49280
	ds_read_b128 v[214:217], v195 offset:57472
	s_waitcnt lgkmcnt(1)
	v_mfma_f32_32x32x16_bf16 v[112:127], v[204:207], v[156:159], v[112:127]
	s_waitcnt lgkmcnt(0)
	v_mfma_f32_32x32x16_bf16 v[96:111], v[214:217], v[156:159], v[96:111]
	ds_read_b128 v[204:207], v196 offset:49280
	ds_read_b128 v[214:217], v196 offset:57472
	s_waitcnt lgkmcnt(1)
	v_mfma_f32_32x32x16_bf16 v[112:127], v[204:207], v[160:163], v[112:127]
	s_waitcnt lgkmcnt(0)
	v_mfma_f32_32x32x16_bf16 v[96:111], v[214:217], v[160:163], v[96:111]
	ds_read_b128 v[204:207], v197 offset:49280
	ds_read_b128 v[214:217], v197 offset:57472
	s_waitcnt lgkmcnt(1)
	v_mfma_f32_32x32x16_bf16 v[112:127], v[204:207], v[164:167], v[112:127]
	s_waitcnt lgkmcnt(0)
	v_mfma_f32_32x32x16_bf16 v[96:111], v[214:217], v[164:167], v[96:111]
	ds_read_b128 v[204:207], v198 offset:49280
	ds_read_b128 v[214:217], v198 offset:57472
	s_waitcnt lgkmcnt(1)
	v_mfma_f32_32x32x16_bf16 v[112:127], v[204:207], v[172:175], v[112:127]
	v_exp_f32_e32 v205, v80
	v_pk_add_f32 v[232:233], v[64:65], v[66:67]
	v_pk_add_f32 v[232:233], v[68:69], v[232:233]
	v_pk_add_f32 v[232:233], v[70:71], v[232:233]
	v_pk_add_f32 v[232:233], v[72:73], v[232:233]
	v_pk_add_f32 v[232:233], v[74:75], v[232:233]
	v_exp_f32_e32 v206, v81
	v_pk_add_f32 v[232:233], v[76:77], v[232:233]
	v_exp_f32_e32 v207, v82
	s_waitcnt lgkmcnt(0)
	v_mfma_f32_32x32x16_bf16 v[96:111], v[214:217], v[172:175], v[96:111]
	v_exp_f32_e32 v214, v83
	v_pk_add_f32 v[232:233], v[78:79], v[232:233]
	v_exp_f32_e32 v215, v84
	v_add_f32_e32 v232, v205, v232
	v_exp_f32_e32 v216, v85
	v_exp_f32_e32 v217, v86
	v_pk_add_f32 v[232:233], v[206:207], v[232:233]
	v_pk_add_f32 v[232:233], v[214:215], v[232:233]
	v_pk_add_f32 v[232:233], v[216:217], v[232:233]
	v_pk_add_f32 v[232:233], v[218:219], v[232:233]
	v_pk_add_f32 v[232:233], v[220:221], v[232:233]
	v_pk_add_f32 v[232:233], v[222:223], v[232:233]
	v_pk_add_f32 v[232:233], v[224:225], v[232:233]
	v_add_f32_e32 v232, v232, v233
	v_add_f32_e32 v203, v95, v232
	v_mov_b32_e32 v204, v203
	v_cvt_pk_bf16_f32 v80, v64, v65
	v_cvt_pk_bf16_f32 v81, v66, v67
	v_cvt_pk_bf16_f32 v82, v68, v69
	v_cvt_pk_bf16_f32 v83, v70, v71
	v_cvt_pk_bf16_f32 v84, v72, v73
	v_cvt_pk_bf16_f32 v85, v74, v75
	v_cvt_pk_bf16_f32 v86, v76, v77
	v_cvt_pk_bf16_f32 v87, v78, v79
	v_cvt_pk_bf16_f32 v88, v205, v206
	v_cvt_pk_bf16_f32 v89, v207, v214
	v_cvt_pk_bf16_f32 v90, v215, v216
	v_cvt_pk_bf16_f32 v91, v217, v218
	v_cvt_pk_bf16_f32 v92, v219, v220
	v_cvt_pk_bf16_f32 v93, v221, v222
	v_cvt_pk_bf16_f32 v94, v223, v224
	v_cvt_pk_bf16_f32 v95, v225, v95
	s_nop 1
	v_permlane32_swap_b32_e32 v203, v204
	v_permlane32_swap_b32_e32 v80, v82
	v_permlane32_swap_b32_e32 v81, v83
	v_permlane32_swap_b32_e32 v84, v86
	v_permlane32_swap_b32_e32 v85, v87
	v_permlane32_swap_b32_e32 v88, v90
	v_permlane32_swap_b32_e32 v89, v91
	v_permlane32_swap_b32_e32 v92, v94
	v_permlane32_swap_b32_e32 v93, v95
	s_lshr_b32 s72, s2, 2
	s_cmp_lg_u32 s72, s74
	s_cselect_b64 s[68:69], -1, 0
	s_and_b64 vcc, exec, s[68:69]
	s_cbranch_vccnz .LBB0_1220
	s_sub_i32 s2, s78, 64
	s_and_b32 s2, s2, 0xc0
	s_or_b32 s3, s2, 63
	s_cmp_le_u32 s3, s84
	s_cbranch_scc1 .LBB0_1220
	v_subrev_u32_e32 v64, s2, v192
	v_cmp_gt_i32_e64 s[60:61], 26, v64
	v_cmp_gt_i32_e64 s[62:63], 27, v64
	v_cmp_gt_i32_e64 s[58:59], 25, v64
	s_and_b64 s[60:61], s[62:63], s[60:61]
	v_cmp_gt_i32_e64 s[56:57], 24, v64
	s_and_b64 s[58:59], s[60:61], s[58:59]
	v_cmp_gt_i32_e64 s[54:55], 19, v64
	s_and_b64 s[56:57], s[58:59], s[56:57]
	v_cmp_gt_i32_e64 s[52:53], 18, v64
	s_and_b64 s[54:55], s[56:57], s[54:55]
	v_cmp_gt_i32_e64 s[50:51], 17, v64
	s_and_b64 s[52:53], s[54:55], s[52:53]
	v_cmp_gt_i32_e64 s[48:49], 16, v64
	s_and_b64 s[50:51], s[52:53], s[50:51]
	v_cmp_gt_i32_e64 s[46:47], 11, v64
	s_and_b64 s[48:49], s[50:51], s[48:49]
	v_cmp_gt_i32_e64 s[44:45], 10, v64
	s_and_b64 s[46:47], s[48:49], s[46:47]
	v_cmp_gt_i32_e64 s[42:43], 9, v64
	s_and_b64 s[44:45], s[46:47], s[44:45]
	v_cmp_gt_i32_e64 s[40:41], 8, v64
	s_and_b64 s[42:43], s[44:45], s[42:43]
	v_cmp_gt_i32_e64 s[38:39], 3, v64
	s_and_b64 s[40:41], s[42:43], s[40:41]
	v_cmp_gt_i32_e64 s[36:37], 2, v64
	s_and_b64 s[38:39], s[40:41], s[38:39]
	v_cmp_gt_i32_e64 s[34:35], 1, v64
	s_and_b64 s[36:37], s[38:39], s[36:37]
	v_cmp_gt_i32_e64 s[30:31], 0, v64
	s_and_b64 s[34:35], s[36:37], s[34:35]
	s_and_b64 s[30:31], s[34:35], s[30:31]
	v_cmp_gt_i32_e64 s[28:29], 58, v64
	v_cndmask_b32_e64 v112, v112, v210, s[30:31]
	v_cmp_gt_i32_e64 s[30:31], 59, v64
	v_cmp_gt_i32_e64 s[26:27], 57, v64
	s_and_b64 s[28:29], s[30:31], s[28:29]
	v_cmp_gt_i32_e64 s[24:25], 56, v64
	s_and_b64 s[26:27], s[28:29], s[26:27]
	v_cmp_gt_i32_e64 s[22:23], 51, v64
	s_and_b64 s[24:25], s[26:27], s[24:25]
	v_cmp_gt_i32_e64 s[20:21], 50, v64
	s_and_b64 s[22:23], s[24:25], s[22:23]
	v_cmp_gt_i32_e64 s[18:19], 49, v64
	s_and_b64 s[20:21], s[22:23], s[20:21]
	v_cmp_gt_i32_e64 s[16:17], 48, v64
	s_and_b64 s[18:19], s[20:21], s[18:19]
	v_cmp_gt_i32_e64 s[14:15], 43, v64
	s_and_b64 s[16:17], s[18:19], s[16:17]
	v_cmp_gt_i32_e64 s[12:13], 42, v64
	s_and_b64 s[14:15], s[16:17], s[14:15]
	v_cmp_gt_i32_e64 s[10:11], 41, v64
	s_and_b64 s[12:13], s[14:15], s[12:13]
	v_cmp_gt_i32_e64 s[8:9], 40, v64
	s_and_b64 s[10:11], s[12:13], s[10:11]
	v_cmp_gt_i32_e64 s[6:7], 35, v64
	s_and_b64 s[8:9], s[10:11], s[8:9]
	v_cmp_gt_i32_e64 s[4:5], 34, v64
	s_and_b64 s[6:7], s[8:9], s[6:7]
	v_cmp_gt_i32_e64 s[2:3], 33, v64
	s_and_b64 s[4:5], s[6:7], s[4:5]
	v_cmp_gt_i32_e32 vcc, 32, v64
	s_and_b64 s[2:3], s[4:5], s[2:3]
	s_and_b64 vcc, s[2:3], vcc
	v_cndmask_b32_e64 v127, v127, v210, s[62:63]
	v_cndmask_b32_e64 v126, v126, v210, s[60:61]
	v_cndmask_b32_e64 v125, v125, v210, s[58:59]
	v_cndmask_b32_e64 v124, v124, v210, s[56:57]
	v_cndmask_b32_e64 v123, v123, v210, s[54:55]
	v_cndmask_b32_e64 v122, v122, v210, s[52:53]
	v_cndmask_b32_e64 v121, v121, v210, s[50:51]
	v_cndmask_b32_e64 v120, v120, v210, s[48:49]
	v_cndmask_b32_e64 v119, v119, v210, s[46:47]
	v_cndmask_b32_e64 v118, v118, v210, s[44:45]
	v_cndmask_b32_e64 v117, v117, v210, s[42:43]
	v_cndmask_b32_e64 v116, v116, v210, s[40:41]
	v_cndmask_b32_e64 v115, v115, v210, s[38:39]
	v_cndmask_b32_e64 v114, v114, v210, s[36:37]
	v_cndmask_b32_e64 v113, v113, v210, s[34:35]
	v_cndmask_b32_e64 v111, v111, v210, s[30:31]
	v_cndmask_b32_e64 v110, v110, v210, s[28:29]
	v_cndmask_b32_e64 v109, v109, v210, s[26:27]
	v_cndmask_b32_e64 v108, v108, v210, s[24:25]
	v_cndmask_b32_e64 v107, v107, v210, s[22:23]
	v_cndmask_b32_e64 v106, v106, v210, s[20:21]
	v_cndmask_b32_e64 v105, v105, v210, s[18:19]
	v_cndmask_b32_e64 v104, v104, v210, s[16:17]
	v_cndmask_b32_e64 v103, v103, v210, s[14:15]
	v_cndmask_b32_e64 v102, v102, v210, s[12:13]
	v_cndmask_b32_e64 v101, v101, v210, s[10:11]
	v_cndmask_b32_e64 v100, v100, v210, s[8:9]
	v_cndmask_b32_e64 v99, v99, v210, s[6:7]
	v_cndmask_b32_e64 v98, v98, v210, s[4:5]
	v_cndmask_b32_e64 v97, v97, v210, s[2:3]
	v_cndmask_b32_e32 v96, v96, v210, vcc
.LBB0_1220:
	s_lshl_b32 s2, 1, s72
	v_and_b32_e32 v64, s2, v193
	v_cmp_eq_u32_e32 vcc, 0, v64
	ds_read_b64_tr_b16 v[64:65], v187 offset:0
	ds_read_b64_tr_b16 v[66:67], v187 offset:0x800
	ds_read_b64_tr_b16 v[68:69], v187 offset:0x1000
	ds_read_b64_tr_b16 v[70:71], v187 offset:0x1800
	ds_read_b64_tr_b16 v[72:73], v187 offset:0x2000
	ds_read_b64_tr_b16 v[74:75], v187 offset:0x2800
	ds_read_b64_tr_b16 v[76:77], v187 offset:0x3000
	ds_read_b64_tr_b16 v[78:79], v187 offset:0x3800
	s_waitcnt lgkmcnt(0)
	s_and_b64 vcc, s[68:69], vcc
	ds_read_b64_tr_b16 v[214:215], v187 offset:0x200
	ds_read_b64_tr_b16 v[216:217], v187 offset:0xa00
	ds_read_b64_tr_b16 v[218:219], v187 offset:0x1200
	ds_read_b64_tr_b16 v[220:221], v187 offset:0x1a00
	ds_read_b64_tr_b16 v[222:223], v187 offset:0x2200
	ds_read_b64_tr_b16 v[224:225], v187 offset:0x2a00
	ds_read_b64_tr_b16 v[226:227], v187 offset:0x3200
	ds_read_b64_tr_b16 v[228:229], v187 offset:0x3a00
	v_mfma_f32_32x32x16_bf16 v[32:47], v[80:83], v[64:67], v[32:47]
	v_max_f32_e32 v64, v113, v113
	v_max_f32_e32 v65, v112, v112
	v_max_f32_e32 v64, v65, v64
	v_max3_f32 v64, v64, v114, v115
	v_max3_f32 v64, v64, v116, v117
	v_max3_f32 v64, v64, v118, v119
	v_max3_f32 v64, v64, v120, v121
	v_mfma_f32_32x32x16_bf16 v[32:47], v[84:87], v[68:71], v[32:47]
	v_max3_f32 v64, v64, v122, v123
	v_max3_f32 v64, v64, v124, v125
	v_max3_f32 v64, v64, v126, v127
	v_max3_f32 v64, v64, v96, v97
	v_max3_f32 v64, v64, v98, v99
	v_max3_f32 v64, v64, v100, v101
	v_max3_f32 v64, v64, v102, v103
	v_mfma_f32_32x32x16_bf16 v[32:47], v[88:91], v[72:75], v[32:47]
	v_max3_f32 v64, v64, v104, v105
	v_max3_f32 v64, v64, v106, v107
	v_max3_f32 v64, v64, v108, v109
	v_max3_f32 v205, v64, v110, v111
	v_mfma_f32_32x32x16_bf16 v[32:47], v[92:95], v[76:79], v[32:47]
	s_waitcnt lgkmcnt(0)
	ds_read_b64_tr_b16 v[64:65], v187 offset:0x400
	ds_read_b64_tr_b16 v[66:67], v187 offset:0xc00
	ds_read_b64_tr_b16 v[68:69], v187 offset:0x1400
	ds_read_b64_tr_b16 v[70:71], v187 offset:0x1c00
	ds_read_b64_tr_b16 v[72:73], v187 offset:0x2400
	ds_read_b64_tr_b16 v[74:75], v187 offset:0x2c00
	ds_read_b64_tr_b16 v[76:77], v187 offset:0x3400
	ds_read_b64_tr_b16 v[78:79], v187 offset:0x3c00
	v_mfma_f32_32x32x16_bf16 v[48:63], v[80:83], v[214:217], v[48:63]
	v_mov_b32_e32 v206, v205
	s_nop 1
	v_permlane32_swap_b32_e32 v205, v206
	v_max_f32_e32 v206, v206, v206
	v_max_f32_e32 v205, v205, v205
	v_max_f32_e32 v205, v205, v206
	v_cndmask_b32_e32 v205, v205, v210, vcc
	v_mfma_f32_32x32x16_bf16 v[48:63], v[84:87], v[218:221], v[48:63]
	v_max_f32_e32 v207, v202, v202
	v_sub_f32_e32 v206, v205, v202
	v_max_f32_e32 v205, v207, v205
	v_mul_f32_e32 v206, 0x3db504f3, v206
	v_sub_f32_e32 v207, v202, v205
	v_cmp_ge_f32_e64 s[2:3], s97, v206
	v_mul_f32_e32 v206, 0x3e0293ee, v207
	v_mfma_f32_32x32x16_bf16 v[48:63], v[88:91], v[222:225], v[48:63]
	v_exp_f32_e32 v207, v206
	s_cmp_eq_u64 s[2:3], exec
	s_cselect_b64 s[2:3], -1, 0
	v_cndmask_b32_e64 v206, v205, v202, s[2:3]
	v_cndmask_b32_e64 v205, v207, 1.0, s[2:3]
	v_mul_f32_e32 v202, 0xbe0293ee, v206
	v_cndmask_b32_e32 v202, v202, v210, vcc
	v_mfma_f32_32x32x16_bf16 v[48:63], v[92:95], v[226:229], v[48:63]
	s_waitcnt lgkmcnt(0)
	ds_read_b64_tr_b16 v[214:215], v187 offset:0x600
	ds_read_b64_tr_b16 v[216:217], v187 offset:0xe00
	ds_read_b64_tr_b16 v[218:219], v187 offset:0x1600
	ds_read_b64_tr_b16 v[220:221], v187 offset:0x1e00
	ds_read_b64_tr_b16 v[222:223], v187 offset:0x2600
	ds_read_b64_tr_b16 v[224:225], v187 offset:0x2e00
	ds_read_b64_tr_b16 v[226:227], v187 offset:0x3600
	ds_read_b64_tr_b16 v[228:229], v187 offset:0x3e00
	v_mfma_f32_32x32x16_bf16 v[16:31], v[80:83], v[64:67], v[16:31]
	v_pk_fma_f32 v[66:67], v[114:115], s[86:87], v[202:203] op_sel_hi:[1,0,0]
	v_pk_fma_f32 v[64:65], v[112:113], s[86:87], v[202:203] op_sel_hi:[1,0,0]
	v_pk_fma_f32 v[110:111], v[110:111], s[86:87], v[202:203] op_sel_hi:[1,0,0]
	v_pk_fma_f32 v[108:109], v[108:109], s[86:87], v[202:203] op_sel_hi:[1,0,0]
	v_pk_fma_f32 v[106:107], v[106:107], s[86:87], v[202:203] op_sel_hi:[1,0,0]
	v_pk_fma_f32 v[104:105], v[104:105], s[86:87], v[202:203] op_sel_hi:[1,0,0]
	v_pk_fma_f32 v[102:103], v[102:103], s[86:87], v[202:203] op_sel_hi:[1,0,0]
	v_mfma_f32_32x32x16_bf16 v[16:31], v[84:87], v[68:71], v[16:31]
	v_pk_fma_f32 v[70:71], v[118:119], s[86:87], v[202:203] op_sel_hi:[1,0,0]
	v_pk_fma_f32 v[68:69], v[116:117], s[86:87], v[202:203] op_sel_hi:[1,0,0]
	v_pk_fma_f32 v[100:101], v[100:101], s[86:87], v[202:203] op_sel_hi:[1,0,0]
	v_pk_fma_f32 v[98:99], v[98:99], s[86:87], v[202:203] op_sel_hi:[1,0,0]
	v_pk_fma_f32 v[96:97], v[96:97], s[86:87], v[202:203] op_sel_hi:[1,0,0]
	v_mfma_f32_32x32x16_bf16 v[16:31], v[88:91], v[72:75], v[16:31]
	v_pk_fma_f32 v[74:75], v[122:123], s[86:87], v[202:203] op_sel_hi:[1,0,0]
	v_pk_fma_f32 v[72:73], v[120:121], s[86:87], v[202:203] op_sel_hi:[1,0,0]
	v_mfma_f32_32x32x16_bf16 v[16:31], v[92:95], v[76:79], v[16:31]
	v_pk_fma_f32 v[78:79], v[126:127], s[86:87], v[202:203] op_sel_hi:[1,0,0]
	v_pk_fma_f32 v[76:77], v[124:125], s[86:87], v[202:203] op_sel_hi:[1,0,0]
	s_waitcnt lgkmcnt(0)
	v_mfma_f32_32x32x16_bf16 v[0:15], v[80:83], v[214:217], v[0:15]
	v_exp_f32_e32 v112, v64
	v_exp_f32_e32 v113, v65
	v_exp_f32_e32 v114, v66
	v_exp_f32_e32 v115, v67
	v_exp_f32_e32 v116, v68
	v_exp_f32_e32 v117, v69
	v_exp_f32_e32 v118, v70
	v_mfma_f32_32x32x16_bf16 v[0:15], v[84:87], v[218:221], v[0:15]
	v_exp_f32_e32 v119, v71
	v_exp_f32_e32 v120, v72
	v_exp_f32_e32 v121, v73
	v_exp_f32_e32 v122, v74
	v_exp_f32_e32 v123, v75
	v_exp_f32_e32 v124, v76
	v_exp_f32_e32 v125, v77
	v_mfma_f32_32x32x16_bf16 v[0:15], v[88:91], v[222:225], v[0:15]
	v_exp_f32_e32 v126, v78
	v_exp_f32_e32 v127, v79
	s_barrier
	s_waitcnt vmcnt(0)
	v_mfma_f32_32x32x16_bf16 v[0:15], v[92:95], v[226:229], v[0:15]
	v_cmp_gt_f32_e32 vcc, 1.0, v205
	s_waitcnt vmcnt(3)
	ds_write_b128 v199, v[130:133]
	s_waitcnt vmcnt(2)
	ds_write_b128 v200, v[134:137]
	s_waitcnt vmcnt(1)
	ds_write_b128 v190, v[168:171] offset:32768
	s_waitcnt vmcnt(0)
	ds_write_b128 v190, v[176:179] offset:40960
	s_cbranch_vccz .LBB0_1224
	s_and_saveexec_b64 s[2:3], s[0:1]
	ds_write_b32 v189, v205 offset:128
	s_or_b64 exec, exec, s[2:3]
	s_waitcnt lgkmcnt(0)
	ds_read_b128 v[64:67], v188 offset:224
	ds_read_b128 v[68:71], v188 offset:192
	ds_read_b128 v[72:75], v188 offset:160
	ds_read_b128 v[76:79], v188 offset:128
	s_waitcnt lgkmcnt(3)
	v_pk_mul_f32 v[46:47], v[46:47], v[66:67]
	s_waitcnt lgkmcnt(2)
	v_pk_mul_f32 v[42:43], v[42:43], v[70:71]
	s_waitcnt lgkmcnt(1)
	v_pk_mul_f32 v[38:39], v[38:39], v[74:75]
	s_waitcnt lgkmcnt(0)
	v_pk_mul_f32 v[34:35], v[34:35], v[78:79]
	v_pk_mul_f32 v[44:45], v[44:45], v[64:65]
	v_pk_mul_f32 v[40:41], v[40:41], v[68:69]
	v_pk_mul_f32 v[36:37], v[36:37], v[72:73]
	v_pk_mul_f32 v[32:33], v[32:33], v[76:77]
	v_pk_mul_f32 v[62:63], v[62:63], v[66:67]
	v_pk_mul_f32 v[58:59], v[58:59], v[70:71]
	v_pk_mul_f32 v[54:55], v[54:55], v[74:75]
	v_pk_mul_f32 v[50:51], v[50:51], v[78:79]
	v_pk_mul_f32 v[60:61], v[60:61], v[64:65]
	v_pk_mul_f32 v[56:57], v[56:57], v[68:69]
	v_pk_mul_f32 v[52:53], v[52:53], v[72:73]
	v_pk_mul_f32 v[48:49], v[48:49], v[76:77]
	v_pk_mul_f32 v[30:31], v[30:31], v[66:67]
	v_pk_mul_f32 v[26:27], v[26:27], v[70:71]
	v_pk_mul_f32 v[22:23], v[22:23], v[74:75]
	v_pk_mul_f32 v[18:19], v[18:19], v[78:79]
	v_pk_mul_f32 v[28:29], v[28:29], v[64:65]
	v_pk_mul_f32 v[24:25], v[24:25], v[68:69]
	v_pk_mul_f32 v[20:21], v[20:21], v[72:73]
	v_pk_mul_f32 v[16:17], v[16:17], v[76:77]
	v_pk_mul_f32 v[14:15], v[14:15], v[66:67]
	v_pk_mul_f32 v[10:11], v[10:11], v[70:71]
	v_pk_mul_f32 v[6:7], v[6:7], v[74:75]
	v_pk_mul_f32 v[2:3], v[2:3], v[78:79]
	v_pk_mul_f32 v[12:13], v[12:13], v[64:65]
	v_pk_mul_f32 v[8:9], v[8:9], v[68:69]
	v_pk_mul_f32 v[4:5], v[4:5], v[72:73]
	v_pk_mul_f32 v[0:1], v[0:1], v[76:77]

.LBB0_1226:
	ds_read_b128 v[64:67], v195 offset:32768
	ds_read_b128 v[68:71], v195 offset:40960
	ds_read_b128 v[214:217], v196 offset:32768
	ds_read_b128 v[218:221], v196 offset:40960
	s_waitcnt lgkmcnt(3)
	v_mfma_f32_32x32x16_bf16 v[80:95], v[64:67], v[140:143], 0
	v_pk_add_f32 v[138:139], v[112:113], v[114:115]
	v_pk_add_f32 v[138:139], v[116:117], v[138:139]
	v_pk_add_f32 v[138:139], v[118:119], v[138:139]
	s_waitcnt lgkmcnt(2)
	v_mfma_f32_32x32x16_bf16 v[64:79], v[68:71], v[140:143], 0
	v_pk_add_f32 v[138:139], v[120:121], v[138:139]
	v_pk_add_f32 v[138:139], v[122:123], v[138:139]
	v_exp_f32_e32 v96, v96
	v_exp_f32_e32 v97, v97
	v_pk_add_f32 v[138:139], v[124:125], v[138:139]
	s_waitcnt lgkmcnt(1)
	v_mfma_f32_32x32x16_bf16 v[80:95], v[214:217], v[144:147], v[80:95]
	v_exp_f32_e32 v98, v98
	v_exp_f32_e32 v99, v99
	v_pk_add_f32 v[138:139], v[126:127], v[138:139]
	v_exp_f32_e32 v100, v100
	v_exp_f32_e32 v101, v101
	s_waitcnt lgkmcnt(0)
	v_mfma_f32_32x32x16_bf16 v[64:79], v[218:221], v[144:147], v[64:79]
	ds_read_b128 v[214:217], v197 offset:32768
	ds_read_b128 v[218:221], v197 offset:40960
	v_pk_add_f32 v[138:139], v[96:97], v[138:139]
	v_exp_f32_e32 v102, v102
	v_exp_f32_e32 v103, v103
	v_pk_add_f32 v[138:139], v[98:99], v[138:139]
	v_exp_f32_e32 v104, v104
	s_waitcnt lgkmcnt(1)
	v_mfma_f32_32x32x16_bf16 v[80:95], v[214:217], v[148:151], v[80:95]
	v_exp_f32_e32 v105, v105
	v_pk_add_f32 v[138:139], v[100:101], v[138:139]
	v_exp_f32_e32 v106, v106
	v_exp_f32_e32 v107, v107
	v_pk_add_f32 v[138:139], v[102:103], v[138:139]
	s_waitcnt lgkmcnt(0)
	v_mfma_f32_32x32x16_bf16 v[64:79], v[218:221], v[148:151], v[64:79]
	ds_read_b128 v[214:217], v198 offset:32768
	ds_read_b128 v[218:221], v198 offset:40960
	v_exp_f32_e32 v108, v108
	v_exp_f32_e32 v109, v109
	v_pk_add_f32 v[138:139], v[104:105], v[138:139]
	v_exp_f32_e32 v110, v110
	s_waitcnt lgkmcnt(1)
	v_mfma_f32_32x32x16_bf16 v[80:95], v[214:217], v[152:155], v[80:95]
	v_exp_f32_e32 v111, v111
	v_pk_add_f32 v[138:139], v[106:107], v[138:139]
	v_pk_add_f32 v[138:139], v[108:109], v[138:139]
	v_pk_add_f32 v[138:139], v[110:111], v[138:139]
	v_add_f32_e32 v138, v138, v139
	v_mov_b32_e32 v139, v138
	s_waitcnt lgkmcnt(0)
	v_mfma_f32_32x32x16_bf16 v[64:79], v[218:221], v[152:155], v[64:79]
	ds_read_b128 v[214:217], v195 offset:32896
	ds_read_b128 v[218:221], v195 offset:41088
	v_permlane32_swap_b32_e32 v138, v139
	s_add_i32 s2, s77, -1
	s_waitcnt lgkmcnt(1)
	v_mfma_f32_32x32x16_bf16 v[80:95], v[214:217], v[156:159], v[80:95]
	s_waitcnt lgkmcnt(0)
	v_mfma_f32_32x32x16_bf16 v[64:79], v[218:221], v[156:159], v[64:79]
	ds_read_b128 v[214:217], v196 offset:32896
	ds_read_b128 v[218:221], v196 offset:41088
	s_waitcnt lgkmcnt(1)
	v_mfma_f32_32x32x16_bf16 v[80:95], v[214:217], v[160:163], v[80:95]
	s_waitcnt lgkmcnt(0)
	v_mfma_f32_32x32x16_bf16 v[64:79], v[218:221], v[160:163], v[64:79]
	ds_read_b128 v[214:217], v197 offset:32896
	ds_read_b128 v[218:221], v197 offset:41088
	s_waitcnt lgkmcnt(1)
	v_mfma_f32_32x32x16_bf16 v[80:95], v[214:217], v[164:167], v[80:95]
	s_waitcnt lgkmcnt(0)
	v_mfma_f32_32x32x16_bf16 v[64:79], v[218:221], v[164:167], v[64:79]
	ds_read_b128 v[214:217], v198 offset:32896
	ds_read_b128 v[218:221], v198 offset:41088
	v_cvt_pk_bf16_f32 v112, v112, v113
	v_cvt_pk_bf16_f32 v113, v114, v115
	v_cvt_pk_bf16_f32 v114, v116, v117
	v_cvt_pk_bf16_f32 v115, v118, v119
	v_cvt_pk_bf16_f32 v116, v120, v121
	v_cvt_pk_bf16_f32 v117, v122, v123
	s_waitcnt lgkmcnt(1)
	v_mfma_f32_32x32x16_bf16 v[80:95], v[214:217], v[172:175], v[80:95]
	v_cvt_pk_bf16_f32 v118, v124, v125
	v_cvt_pk_bf16_f32 v119, v126, v127
	v_cvt_pk_bf16_f32 v120, v96, v97
	v_cvt_pk_bf16_f32 v121, v98, v99
	v_cvt_pk_bf16_f32 v122, v100, v101
	v_cvt_pk_bf16_f32 v123, v102, v103
	v_cvt_pk_bf16_f32 v124, v104, v105
	s_waitcnt lgkmcnt(0)
	v_mfma_f32_32x32x16_bf16 v[64:79], v[218:221], v[172:175], v[64:79]
	v_cvt_pk_bf16_f32 v125, v106, v107
	v_cvt_pk_bf16_f32 v126, v108, v109
	v_cvt_pk_bf16_f32 v127, v110, v111
	v_permlane32_swap_b32_e32 v112, v114
	v_permlane32_swap_b32_e32 v113, v115
	v_permlane32_swap_b32_e32 v116, v118
	v_permlane32_swap_b32_e32 v117, v119
	v_permlane32_swap_b32_e32 v120, v122
	v_permlane32_swap_b32_e32 v121, v123
	v_permlane32_swap_b32_e32 v124, v126
	v_permlane32_swap_b32_e32 v125, v127
	s_lshr_b32 s90, s2, 2
	s_cmp_lg_u32 s90, s74
	s_cselect_b64 s[72:73], -1, 0
	s_and_b64 vcc, exec, s[72:73]
	s_cbranch_vccnz .LBB0_1229
	s_and_b32 s2, s78, 0xc0
	s_or_b32 s3, s2, 63
	s_cmp_le_u32 s3, s84
	s_cbranch_scc1 .LBB0_1229
	v_subrev_u32_e32 v96, s2, v192
	v_cmp_gt_i32_e64 s[60:61], 26, v96
	v_cmp_gt_i32_e64 s[62:63], 27, v96
	v_cmp_gt_i32_e64 s[58:59], 25, v96
	s_and_b64 s[60:61], s[62:63], s[60:61]
	v_cmp_gt_i32_e64 s[56:57], 24, v96
	s_and_b64 s[58:59], s[60:61], s[58:59]
	v_cmp_gt_i32_e64 s[54:55], 19, v96
	s_and_b64 s[56:57], s[58:59], s[56:57]
	v_cmp_gt_i32_e64 s[52:53], 18, v96
	s_and_b64 s[54:55], s[56:57], s[54:55]
	v_cmp_gt_i32_e64 s[50:51], 17, v96
	s_and_b64 s[52:53], s[54:55], s[52:53]
	v_cmp_gt_i32_e64 s[48:49], 16, v96
	s_and_b64 s[50:51], s[52:53], s[50:51]
	v_cmp_gt_i32_e64 s[46:47], 11, v96
	s_and_b64 s[48:49], s[50:51], s[48:49]
	v_cmp_gt_i32_e64 s[44:45], 10, v96
	s_and_b64 s[46:47], s[48:49], s[46:47]
	v_cmp_gt_i32_e64 s[42:43], 9, v96
	s_and_b64 s[44:45], s[46:47], s[44:45]
	v_cmp_gt_i32_e64 s[40:41], 8, v96
	s_and_b64 s[42:43], s[44:45], s[42:43]
	v_cmp_gt_i32_e64 s[38:39], 3, v96
	s_and_b64 s[40:41], s[42:43], s[40:41]
	v_cmp_gt_i32_e64 s[36:37], 2, v96
	s_and_b64 s[38:39], s[40:41], s[38:39]
	v_cmp_gt_i32_e64 s[34:35], 1, v96
	s_and_b64 s[36:37], s[38:39], s[36:37]
	v_cmp_gt_i32_e64 s[30:31], 0, v96
	s_and_b64 s[34:35], s[36:37], s[34:35]
	s_and_b64 s[30:31], s[34:35], s[30:31]
	v_cmp_gt_i32_e64 s[28:29], 58, v96
	v_cndmask_b32_e64 v80, v80, v210, s[30:31]
	v_cmp_gt_i32_e64 s[30:31], 59, v96
	v_cmp_gt_i32_e64 s[26:27], 57, v96
	s_and_b64 s[28:29], s[30:31], s[28:29]
	v_cmp_gt_i32_e64 s[24:25], 56, v96
	s_and_b64 s[26:27], s[28:29], s[26:27]
	v_cmp_gt_i32_e64 s[22:23], 51, v96
	s_and_b64 s[24:25], s[26:27], s[24:25]
	v_cmp_gt_i32_e64 s[20:21], 50, v96
	s_and_b64 s[22:23], s[24:25], s[22:23]
	v_cmp_gt_i32_e64 s[18:19], 49, v96
	s_and_b64 s[20:21], s[22:23], s[20:21]
	v_cmp_gt_i32_e64 s[16:17], 48, v96
	s_and_b64 s[18:19], s[20:21], s[18:19]
	v_cmp_gt_i32_e64 s[14:15], 43, v96
	s_and_b64 s[16:17], s[18:19], s[16:17]
	v_cmp_gt_i32_e64 s[12:13], 42, v96
	s_and_b64 s[14:15], s[16:17], s[14:15]
	v_cmp_gt_i32_e64 s[10:11], 41, v96
	s_and_b64 s[12:13], s[14:15], s[12:13]
	v_cmp_gt_i32_e64 s[8:9], 40, v96
	s_and_b64 s[10:11], s[12:13], s[10:11]
	v_cmp_gt_i32_e64 s[6:7], 35, v96
	s_and_b64 s[8:9], s[10:11], s[8:9]
	v_cmp_gt_i32_e64 s[4:5], 34, v96
	s_and_b64 s[6:7], s[8:9], s[6:7]
	v_cmp_gt_i32_e64 s[2:3], 33, v96
	s_and_b64 s[4:5], s[6:7], s[4:5]
	v_cmp_gt_i32_e32 vcc, 32, v96
	s_and_b64 s[2:3], s[4:5], s[2:3]
	s_and_b64 vcc, s[2:3], vcc
	v_cndmask_b32_e64 v95, v95, v210, s[62:63]
	v_cndmask_b32_e64 v94, v94, v210, s[60:61]
	v_cndmask_b32_e64 v93, v93, v210, s[58:59]
	v_cndmask_b32_e64 v92, v92, v210, s[56:57]
	v_cndmask_b32_e64 v91, v91, v210, s[54:55]
	v_cndmask_b32_e64 v90, v90, v210, s[52:53]
	v_cndmask_b32_e64 v89, v89, v210, s[50:51]
	v_cndmask_b32_e64 v88, v88, v210, s[48:49]
	v_cndmask_b32_e64 v87, v87, v210, s[46:47]
	v_cndmask_b32_e64 v86, v86, v210, s[44:45]
	v_cndmask_b32_e64 v85, v85, v210, s[42:43]
	v_cndmask_b32_e64 v84, v84, v210, s[40:41]
	v_cndmask_b32_e64 v83, v83, v210, s[38:39]
	v_cndmask_b32_e64 v82, v82, v210, s[36:37]
	v_cndmask_b32_e64 v81, v81, v210, s[34:35]
	v_cndmask_b32_e64 v79, v79, v210, s[30:31]
	v_cndmask_b32_e64 v78, v78, v210, s[28:29]
	v_cndmask_b32_e64 v77, v77, v210, s[26:27]
	v_cndmask_b32_e64 v76, v76, v210, s[24:25]
	v_cndmask_b32_e64 v75, v75, v210, s[22:23]
	v_cndmask_b32_e64 v74, v74, v210, s[20:21]
	v_cndmask_b32_e64 v73, v73, v210, s[18:19]
	v_cndmask_b32_e64 v72, v72, v210, s[16:17]
	v_cndmask_b32_e64 v71, v71, v210, s[14:15]
	v_cndmask_b32_e64 v70, v70, v210, s[12:13]
	v_cndmask_b32_e64 v69, v69, v210, s[10:11]
	v_cndmask_b32_e64 v68, v68, v210, s[8:9]
	v_cndmask_b32_e64 v67, v67, v210, s[6:7]
	v_cndmask_b32_e64 v66, v66, v210, s[4:5]
	v_cndmask_b32_e64 v65, v65, v210, s[2:3]
	v_cndmask_b32_e32 v64, v64, v210, vcc
.LBB0_1229:
	s_lshl_b32 s2, 1, s90
	v_and_b32_e32 v96, s2, v193
	v_cmp_eq_u32_e32 vcc, 0, v96
	ds_read_b64_tr_b16 v[96:97], v187 offset:0x4000
	ds_read_b64_tr_b16 v[98:99], v187 offset:0x4800
	ds_read_b64_tr_b16 v[100:101], v187 offset:0x5000
	ds_read_b64_tr_b16 v[102:103], v187 offset:0x5800
	ds_read_b64_tr_b16 v[104:105], v187 offset:0x6000
	ds_read_b64_tr_b16 v[106:107], v187 offset:0x6800
	ds_read_b64_tr_b16 v[108:109], v187 offset:0x7000
	ds_read_b64_tr_b16 v[110:111], v187 offset:0x7800
	s_waitcnt lgkmcnt(0)
	s_and_b64 vcc, s[72:73], vcc
	ds_read_b64_tr_b16 v[214:215], v187 offset:0x4200
	ds_read_b64_tr_b16 v[216:217], v187 offset:0x4a00
	ds_read_b64_tr_b16 v[218:219], v187 offset:0x5200
	ds_read_b64_tr_b16 v[220:221], v187 offset:0x5a00
	ds_read_b64_tr_b16 v[222:223], v187 offset:0x6200
	ds_read_b64_tr_b16 v[224:225], v187 offset:0x6a00
	ds_read_b64_tr_b16 v[226:227], v187 offset:0x7200
	ds_read_b64_tr_b16 v[228:229], v187 offset:0x7a00
	v_mfma_f32_32x32x16_bf16 v[32:47], v[112:115], v[96:99], v[32:47]
	v_max_f32_e32 v96, v81, v81
	v_max_f32_e32 v97, v80, v80
	v_max_f32_e32 v96, v97, v96
	v_max3_f32 v96, v96, v82, v83
	v_max3_f32 v96, v96, v84, v85
	v_max3_f32 v96, v96, v86, v87
	v_max3_f32 v96, v96, v88, v89
	v_mfma_f32_32x32x16_bf16 v[32:47], v[116:119], v[100:103], v[32:47]
	v_max3_f32 v96, v96, v90, v91
	v_max3_f32 v96, v96, v92, v93
	v_max3_f32 v96, v96, v94, v95
	v_max3_f32 v96, v96, v64, v65
	v_max3_f32 v96, v96, v66, v67
	v_max3_f32 v96, v96, v68, v69
	v_max3_f32 v96, v96, v70, v71
	v_mfma_f32_32x32x16_bf16 v[32:47], v[120:123], v[104:107], v[32:47]
	v_max3_f32 v96, v96, v72, v73
	v_max3_f32 v96, v96, v74, v75
	v_max3_f32 v96, v96, v76, v77
	v_max3_f32 v182, v96, v78, v79
	v_mfma_f32_32x32x16_bf16 v[32:47], v[124:127], v[108:111], v[32:47]
	s_waitcnt lgkmcnt(0)
	ds_read_b64_tr_b16 v[96:97], v187 offset:0x4400
	ds_read_b64_tr_b16 v[98:99], v187 offset:0x4c00
	ds_read_b64_tr_b16 v[100:101], v187 offset:0x5400
	ds_read_b64_tr_b16 v[102:103], v187 offset:0x5c00
	ds_read_b64_tr_b16 v[104:105], v187 offset:0x6400
	ds_read_b64_tr_b16 v[106:107], v187 offset:0x6c00
	ds_read_b64_tr_b16 v[108:109], v187 offset:0x7400
	ds_read_b64_tr_b16 v[110:111], v187 offset:0x7c00
	v_mfma_f32_32x32x16_bf16 v[48:63], v[112:115], v[214:217], v[48:63]
	v_mov_b32_e32 v183, v182
	s_nop 1
	v_permlane32_swap_b32_e32 v182, v183
	v_max_f32_e32 v183, v183, v183
	v_max_f32_e32 v182, v182, v182
	v_max_f32_e32 v182, v182, v183
	v_cndmask_b32_e32 v182, v182, v210, vcc
	v_mfma_f32_32x32x16_bf16 v[48:63], v[116:119], v[218:221], v[48:63]
	v_sub_f32_e32 v183, v182, v206
	v_mul_f32_e32 v183, 0x3db504f3, v183
	v_cmp_ge_f32_e64 s[2:3], s97, v183
	s_cmp_eq_u64 s[2:3], exec
	v_max_f32_e32 v183, v206, v206
	v_max_f32_e32 v182, v183, v182
	s_cselect_b64 s[2:3], -1, 0
	v_mfma_f32_32x32x16_bf16 v[48:63], v[120:123], v[222:225], v[48:63]
	v_cndmask_b32_e64 v202, v182, v206, s[2:3]
	v_mul_f32_e32 v183, 0xbe0293ee, v202
	v_cndmask_b32_e32 v230, v183, v210, vcc
	v_mfma_f32_32x32x16_bf16 v[48:63], v[124:127], v[226:229], v[48:63]
	s_waitcnt lgkmcnt(0)
	ds_read_b64_tr_b16 v[214:215], v187 offset:0x4600
	ds_read_b64_tr_b16 v[216:217], v187 offset:0x4e00
	ds_read_b64_tr_b16 v[218:219], v187 offset:0x5600
	ds_read_b64_tr_b16 v[220:221], v187 offset:0x5e00
	ds_read_b64_tr_b16 v[222:223], v187 offset:0x6600
	ds_read_b64_tr_b16 v[224:225], v187 offset:0x6e00
	ds_read_b64_tr_b16 v[226:227], v187 offset:0x7600
	ds_read_b64_tr_b16 v[228:229], v187 offset:0x7e00
	v_mfma_f32_32x32x16_bf16 v[16:31], v[112:115], v[96:99], v[16:31]
	v_pk_fma_f32 v[98:99], v[82:83], s[86:87], v[230:231] op_sel_hi:[1,0,0]
	v_pk_fma_f32 v[96:97], v[80:81], s[86:87], v[230:231] op_sel_hi:[1,0,0]
	v_pk_fma_f32 v[82:83], v[66:67], s[86:87], v[230:231] op_sel_hi:[1,0,0]
	v_pk_fma_f32 v[80:81], v[64:65], s[86:87], v[230:231] op_sel_hi:[1,0,0]
	v_mfma_f32_32x32x16_bf16 v[16:31], v[116:119], v[100:103], v[16:31]
	v_pk_fma_f32 v[102:103], v[86:87], s[86:87], v[230:231] op_sel_hi:[1,0,0]
	v_pk_fma_f32 v[100:101], v[84:85], s[86:87], v[230:231] op_sel_hi:[1,0,0]
	v_pk_fma_f32 v[86:87], v[70:71], s[86:87], v[230:231] op_sel_hi:[1,0,0]
	v_pk_fma_f32 v[84:85], v[68:69], s[86:87], v[230:231] op_sel_hi:[1,0,0]
	v_mfma_f32_32x32x16_bf16 v[16:31], v[120:123], v[104:107], v[16:31]
	v_pk_fma_f32 v[106:107], v[90:91], s[86:87], v[230:231] op_sel_hi:[1,0,0]
	v_pk_fma_f32 v[104:105], v[88:89], s[86:87], v[230:231] op_sel_hi:[1,0,0]
	v_pk_fma_f32 v[90:91], v[74:75], s[86:87], v[230:231] op_sel_hi:[1,0,0]
	v_pk_fma_f32 v[88:89], v[72:73], s[86:87], v[230:231] op_sel_hi:[1,0,0]
	v_mfma_f32_32x32x16_bf16 v[16:31], v[124:127], v[108:111], v[16:31]
	v_pk_fma_f32 v[110:111], v[94:95], s[86:87], v[230:231] op_sel_hi:[1,0,0]
	v_pk_fma_f32 v[108:109], v[92:93], s[86:87], v[230:231] op_sel_hi:[1,0,0]
	v_pk_fma_f32 v[94:95], v[78:79], s[86:87], v[230:231] op_sel_hi:[1,0,0]
	v_pk_fma_f32 v[92:93], v[76:77], s[86:87], v[230:231] op_sel_hi:[1,0,0]
	s_nop 0
	s_waitcnt lgkmcnt(0)
	v_mfma_f32_32x32x16_bf16 v[0:15], v[112:115], v[214:217], v[0:15]
	v_exp_f32_e32 v64, v96
	v_exp_f32_e32 v65, v97
	v_exp_f32_e32 v66, v98
	v_exp_f32_e32 v67, v99
	v_exp_f32_e32 v68, v100
	v_exp_f32_e32 v69, v101
	v_exp_f32_e32 v70, v102
	v_mfma_f32_32x32x16_bf16 v[0:15], v[116:119], v[218:221], v[0:15]
	v_exp_f32_e32 v71, v103
	v_exp_f32_e32 v72, v104
	v_exp_f32_e32 v73, v105
	v_exp_f32_e32 v74, v106
	v_exp_f32_e32 v75, v107
	v_exp_f32_e32 v76, v108
	v_exp_f32_e32 v77, v109
	v_mfma_f32_32x32x16_bf16 v[0:15], v[120:123], v[222:225], v[0:15]
	v_exp_f32_e32 v78, v110
	v_exp_f32_e32 v79, v111
	s_andn2_b64 vcc, exec, s[68:69]
	s_barrier
	v_mfma_f32_32x32x16_bf16 v[0:15], v[124:127], v[226:229], v[0:15]
	s_cbranch_vccnz .LBB0_1231
	s_waitcnt vmcnt(0)
	s_waitcnt vmcnt(3)
	ds_write_b128 v199, v[130:133] offset:16384
	s_waitcnt vmcnt(2)
	ds_write_b128 v200, v[134:137] offset:16384
	s_waitcnt vmcnt(1)
	ds_write_b128 v190, v[168:171] offset:49152
	s_waitcnt vmcnt(0)
	ds_write_b128 v190, v[176:179] offset:57344
